# speedup vs baseline: 1.0142x; 1.0142x over previous
_Z6gat_k1PKfS0_S0_S0_PDF16_S1_S1_Pf:
	s_load_dwordx8 s[4:11], s[0:1], 0x0
	v_lshrrev_b32_e32 v54, 6, v0
	v_and_b32_e32 v57, 0xc0, v0
	s_lshl_b32 s3, s2, 5
	v_and_b32_e32 v1, 63, v0
	v_bfe_u32 v55, v0, 5, 1
	v_lshlrev_b32_e32 v2, 8, v57
	v_mov_b32_e32 v19, 0
	v_or_b32_e32 v4, s3, v54
	v_and_b32_e32 v56, 31, v0
	v_lshl_or_b32 v18, v55, 11, v2
	v_lshlrev_b32_e32 v20, 4, v1
	v_mov_b32_e32 v21, v19
	v_ashrrev_i32_e32 v5, 31, v4
	s_waitcnt lgkmcnt(0)
	v_lshl_add_u64 v[2:3], s[6:7], 0, v[18:19]
	v_lshlrev_b32_e32 v18, 2, v56
	v_lshl_add_u64 v[6:7], s[4:5], 0, v[20:21]
	v_lshlrev_b64 v[8:9], 10, v[4:5]
	v_lshl_add_u64 v[2:3], v[2:3], 0, v[18:19]
	v_lshl_add_u64 v[10:11], v[6:7], 0, v[8:9]
	v_or_b32_e32 v12, 0x1000, v8
	v_mov_b32_e32 v13, v9
	global_load_dword v58, v[2:3], off
	global_load_dword v59, v[2:3], off offset:128
	global_load_dword v60, v[2:3], off offset:256
	global_load_dword v61, v[2:3], off offset:384
	global_load_dword v62, v[2:3], off offset:512
	global_load_dword v63, v[2:3], off offset:640
	global_load_dword v64, v[2:3], off offset:768
	global_load_dword v65, v[2:3], off offset:896
	v_lshl_add_u64 v[12:13], v[6:7], 0, v[12:13]
	global_load_dwordx4 v[22:25], v[10:11], off nt
	global_load_dwordx4 v[26:29], v[12:13], off nt
	v_or_b32_e32 v10, 0x2000, v8
	v_mov_b32_e32 v11, v9
	v_or_b32_e32 v8, 0x3000, v8
	v_lshl_add_u64 v[10:11], v[6:7], 0, v[10:11]
	v_lshl_add_u64 v[8:9], v[6:7], 0, v[8:9]
	global_load_dwordx4 v[30:33], v[10:11], off nt
	global_load_dwordx4 v[34:37], v[8:9], off nt
	v_or_b32_e32 v8, 16, v4
	v_ashrrev_i32_e32 v9, 31, v8
	v_or_b32_e32 v10, 20, v4
	v_lshlrev_b64 v[8:9], 10, v[8:9]
	v_ashrrev_i32_e32 v11, 31, v10
	v_lshl_add_u64 v[8:9], v[6:7], 0, v[8:9]
	v_lshlrev_b64 v[10:11], 10, v[10:11]
	v_lshl_add_u64 v[10:11], v[6:7], 0, v[10:11]
	global_load_dwordx4 v[38:41], v[8:9], off nt
	global_load_dwordx4 v[42:45], v[10:11], off nt
	v_or_b32_e32 v8, 24, v4
	v_ashrrev_i32_e32 v9, 31, v8
	v_or_b32_e32 v4, 28, v4
	v_lshlrev_b64 v[8:9], 10, v[8:9]
	v_ashrrev_i32_e32 v5, 31, v4
	v_lshl_add_u64 v[8:9], v[6:7], 0, v[8:9]
	v_lshlrev_b64 v[4:5], 10, v[4:5]
	v_lshl_add_u64 v[4:5], v[6:7], 0, v[4:5]
	global_load_dwordx4 v[46:49], v[8:9], off nt
	global_load_dwordx4 v[50:53], v[4:5], off nt
	global_load_dword v19, v[2:3], off offset:1024
	global_load_dword v66, v[2:3], off offset:1152
	global_load_dword v67, v[2:3], off offset:1280
	global_load_dword v68, v[2:3], off offset:1408
	global_load_dword v69, v[2:3], off offset:1536
	global_load_dword v70, v[2:3], off offset:1664
	global_load_dword v71, v[2:3], off offset:1792
	global_load_dword v72, v[2:3], off offset:1920
	s_movk_i32 s4, 0x1000
	v_add_co_u32_e32 v4, vcc, s4, v2
	s_movk_i32 s4, 0x2000
	s_nop 0
	v_addc_co_u32_e32 v5, vcc, 0, v3, vcc
	v_add_co_u32_e32 v6, vcc, s4, v2
	s_movk_i32 s4, 0x3000
	s_nop 0
	v_addc_co_u32_e32 v7, vcc, 0, v3, vcc
	global_load_dword v73, v[4:5], off offset:128
	global_load_dword v74, v[4:5], off offset:256
	global_load_dword v75, v[4:5], off offset:384
	global_load_dword v76, v[4:5], off offset:512
	global_load_dword v77, v[4:5], off offset:640
	global_load_dword v78, v[4:5], off offset:768
	global_load_dword v79, v[4:5], off offset:896
	global_load_dword v80, v[4:5], off offset:1024
	global_load_dword v81, v[4:5], off offset:1152
	global_load_dword v82, v[4:5], off offset:1280
	global_load_dword v83, v[4:5], off offset:1408
	global_load_dword v84, v[4:5], off offset:1536
	global_load_dword v85, v[4:5], off offset:1664
	global_load_dword v86, v[4:5], off offset:1792
	global_load_dword v87, v[4:5], off offset:1920
	global_load_dword v88, v[6:7], off offset:-4096
	global_load_dword v89, v[6:7], off
	global_load_dword v90, v[6:7], off offset:128
	global_load_dword v91, v[6:7], off offset:256
	global_load_dword v92, v[6:7], off offset:384
	global_load_dword v93, v[6:7], off offset:512
	global_load_dword v94, v[6:7], off offset:640
	global_load_dword v95, v[6:7], off offset:768
	global_load_dword v96, v[6:7], off offset:896
	global_load_dword v97, v[6:7], off offset:1024
	global_load_dword v98, v[6:7], off offset:1152
	global_load_dword v99, v[6:7], off offset:1280
	global_load_dword v100, v[6:7], off offset:1408
	global_load_dword v101, v[6:7], off offset:1536
	global_load_dword v102, v[6:7], off offset:1664
	global_load_dword v103, v[6:7], off offset:1792
	global_load_dword v104, v[6:7], off offset:1920
	v_add_co_u32_e32 v2, vcc, s4, v2
	v_and_b32_e32 v1, 7, v0
	s_nop 0
	v_addc_co_u32_e32 v3, vcc, 0, v3, vcc
	global_load_dword v105, v[2:3], off
	global_load_dword v106, v[2:3], off offset:128
	global_load_dword v107, v[2:3], off offset:256
	global_load_dword v108, v[2:3], off offset:384
	global_load_dword v109, v[2:3], off offset:512
	global_load_dword v110, v[2:3], off offset:640
	global_load_dword v111, v[2:3], off offset:768
	global_load_dword v112, v[2:3], off offset:896
	global_load_dword v113, v[2:3], off offset:1024
	global_load_dword v114, v[2:3], off offset:1152
	global_load_dword v115, v[2:3], off offset:1280
	global_load_dword v116, v[2:3], off offset:1408
	global_load_dword v117, v[2:3], off offset:1536
	global_load_dword v118, v[2:3], off offset:1664
	global_load_dword v119, v[2:3], off offset:1792
	global_load_dword v120, v[2:3], off offset:1920
	v_lshlrev_b32_e32 v121, 5, v1
	global_load_dwordx4 v[6:9], v121, s[8:9]
	global_load_dwordx4 v[2:5], v121, s[10:11]
	global_load_dwordx4 v[14:17], v121, s[8:9] offset:16
	global_load_dwordx4 v[10:13], v121, s[10:11] offset:16
	s_movk_i32 s4, 0x410
	v_mad_u32_u24 v122, v54, s4, v20
	s_movk_i32 s8, 0x110
	s_load_dwordx2 s[4:5], s[0:1], 0x20
	s_waitcnt vmcnt(62)
	ds_write_b128 v122, v[22:25] offset:34816
	ds_write_b128 v122, v[26:29] offset:38976
	ds_write_b128 v122, v[30:33] offset:43136
	ds_write_b128 v122, v[34:37] offset:47296
	ds_write_b128 v122, v[38:41] offset:51456
	ds_write_b128 v122, v[42:45] offset:55616
	s_waitcnt vmcnt(61)
	ds_write_b128 v122, v[46:49] offset:59776
	s_waitcnt vmcnt(60)
	ds_write_b128 v122, v[50:53] offset:63936
	v_mul_u32_u24_e32 v22, 0x410, v56
	v_lshlrev_b32_e32 v23, 2, v57
	v_and_b32_e32 v24, 32, v0
	v_add3_u32 v38, v22, v23, v24
	s_waitcnt lgkmcnt(0)
	s_barrier
	ds_read_b128 v[22:25], v38 offset:34832
	ds_read_b128 v[26:29], v38 offset:34816
	ds_read_b128 v[30:33], v38 offset:34880
	ds_read_b128 v[34:37], v38 offset:34896
	s_waitcnt lgkmcnt(3)
	v_cvt_pk_f16_f32 v25, v24, v25
	v_cvt_pk_f16_f32 v24, v22, v23
	s_waitcnt lgkmcnt(2)
	v_cvt_pk_f16_f32 v23, v28, v29
	v_cvt_pk_f16_f32 v22, v26, v27
	s_waitcnt vmcnt(53)
	v_cvt_pk_f16_f32 v29, v69, v71
	v_cvt_pk_f16_f32 v28, v19, v67
	v_cvt_pk_f16_f32 v27, v62, v64
	v_cvt_pk_f16_f32 v26, v58, v60
	v_lshlrev_b32_e32 v19, 2, v55
	s_nop 0
	v_mfma_f32_32x32x16_f16 a[0:15], v[22:25], v[26:29], 0
	s_waitcnt vmcnt(52)
	v_cvt_pk_f16_f32 v29, v70, v72
	v_cvt_pk_f16_f32 v28, v66, v68
	v_cvt_pk_f16_f32 v27, v63, v65
	v_cvt_pk_f16_f32 v26, v59, v61
	s_nop 1
	v_mfma_f32_32x32x16_f16 a[16:31], v[22:25], v[26:29], 0
	s_waitcnt lgkmcnt(0)
	v_cvt_pk_f16_f32 v25, v36, v37
	v_cvt_pk_f16_f32 v24, v34, v35
	v_cvt_pk_f16_f32 v23, v32, v33
	v_cvt_pk_f16_f32 v22, v30, v31
	ds_read_b128 v[30:33], v38 offset:34944
	ds_read_b128 v[34:37], v38 offset:34960
	s_waitcnt vmcnt(38)
	v_cvt_pk_f16_f32 v29, v84, v86
	v_cvt_pk_f16_f32 v28, v80, v82
	v_cvt_pk_f16_f32 v27, v76, v78
	s_waitcnt vmcnt(36)
	v_cvt_pk_f16_f32 v26, v88, v74
	s_nop 1
	v_mfma_f32_32x32x16_f16 a[0:15], v[22:25], v[26:29], a[0:15]
	v_cvt_pk_f16_f32 v29, v85, v87
	v_cvt_pk_f16_f32 v28, v81, v83
	v_cvt_pk_f16_f32 v27, v77, v79
	v_cvt_pk_f16_f32 v26, v73, v75
	s_nop 1
	v_mfma_f32_32x32x16_f16 a[16:31], v[22:25], v[26:29], a[16:31]
	s_waitcnt lgkmcnt(0)
	v_cvt_pk_f16_f32 v25, v36, v37
	v_cvt_pk_f16_f32 v24, v34, v35
	v_cvt_pk_f16_f32 v23, v32, v33
	v_cvt_pk_f16_f32 v22, v30, v31
	ds_read_b128 v[30:33], v38 offset:35008
	ds_read_b128 v[34:37], v38 offset:35024
	s_waitcnt vmcnt(21)
	v_cvt_pk_f16_f32 v29, v101, v103
	v_cvt_pk_f16_f32 v28, v97, v99
	v_cvt_pk_f16_f32 v27, v93, v95
	v_cvt_pk_f16_f32 v26, v89, v91
	s_nop 1
	v_mfma_f32_32x32x16_f16 a[0:15], v[22:25], v[26:29], a[0:15]
	s_waitcnt vmcnt(20)
	v_cvt_pk_f16_f32 v29, v102, v104
	v_cvt_pk_f16_f32 v28, v98, v100
	v_cvt_pk_f16_f32 v27, v94, v96
	v_cvt_pk_f16_f32 v26, v90, v92
	s_nop 1
	v_mfma_f32_32x32x16_f16 a[16:31], v[22:25], v[26:29], a[16:31]
	s_waitcnt lgkmcnt(0)
	v_cvt_pk_f16_f32 v25, v36, v37
	v_cvt_pk_f16_f32 v24, v34, v35
	v_cvt_pk_f16_f32 v23, v32, v33
	v_cvt_pk_f16_f32 v22, v30, v31
	s_waitcnt vmcnt(5)
	v_cvt_pk_f16_f32 v29, v117, v119
	v_cvt_pk_f16_f32 v28, v113, v115
	v_cvt_pk_f16_f32 v27, v109, v111
	v_cvt_pk_f16_f32 v26, v105, v107
	s_nop 1
	v_mfma_f32_32x32x16_f16 a[0:15], v[22:25], v[26:29], a[0:15]
	s_waitcnt vmcnt(4)
	v_cvt_pk_f16_f32 v29, v118, v120
	v_cvt_pk_f16_f32 v28, v114, v116
	v_cvt_pk_f16_f32 v27, v110, v112
	v_cvt_pk_f16_f32 v26, v106, v108
	s_nop 1
	v_mfma_f32_32x32x16_f16 a[16:31], v[22:25], v[26:29], a[16:31]
	v_lshl_or_b32 v22, v54, 5, v19
	v_mul_u32_u24_e32 v22, 0x44, v22
	v_lshl_add_u32 v22, v22, 2, v18
	s_nop 0
	ds_write_b32 v22, a0
	s_nop 6
	ds_write_b32 v22, a16 offset:128
	ds_write_b32 v22, a1 offset:272
	ds_write_b32 v22, a17 offset:400
	ds_write_b32 v22, a2 offset:544
	ds_write_b32 v22, a18 offset:672
	ds_write_b32 v22, a3 offset:816
	ds_write_b32 v22, a19 offset:944
	ds_write_b32 v22, a4 offset:2176
	ds_write_b32 v22, a20 offset:2304
	ds_write_b32 v22, a5 offset:2448
	ds_write_b32 v22, a21 offset:2576
	ds_write_b32 v22, a6 offset:2720
	ds_write_b32 v22, a22 offset:2848
	ds_write_b32 v22, a7 offset:2992
	ds_write_b32 v22, a23 offset:3120
	ds_write_b32 v22, a8 offset:4352
	ds_write_b32 v22, a24 offset:4480
	ds_write_b32 v22, a9 offset:4624
	ds_write_b32 v22, a25 offset:4752
	ds_write_b32 v22, a10 offset:4896
	ds_write_b32 v22, a26 offset:5024
	ds_write_b32 v22, a11 offset:5168
	ds_write_b32 v22, a27 offset:5296
	ds_write_b32 v22, a12 offset:6528
	ds_write_b32 v22, a28 offset:6656
	ds_write_b32 v22, a13 offset:6800
	ds_write_b32 v22, a29 offset:6928
	ds_write_b32 v22, a14 offset:7072
	ds_write_b32 v22, a30 offset:7200
	ds_write_b32 v22, a15 offset:7344
	ds_write_b32 v22, a31 offset:7472
	v_lshrrev_b32_e32 v22, 3, v0
	v_mad_u32_u24 v23, v22, s8, v121
	s_waitcnt lgkmcnt(0)
	s_barrier
	ds_read_b128 v[24:27], v23
	ds_read_b128 v[28:31], v23 offset:16
	ds_read_b128 v[32:35], v23 offset:8704
	s_waitcnt lgkmcnt(2)
	v_pk_add_f32 v[36:37], v[26:27], 0 op_sel_hi:[1,0]
	v_pk_add_f32 v[38:39], v[24:25], 0 op_sel_hi:[1,0]
	ds_read_b128 v[24:27], v23 offset:8720
	s_waitcnt lgkmcnt(2)
	v_pk_add_f32 v[40:41], v[30:31], 0 op_sel_hi:[1,0]
	v_pk_add_f32 v[42:43], v[28:29], 0 op_sel_hi:[1,0]
	ds_read_b128 v[28:31], v23 offset:17408
	s_waitcnt lgkmcnt(2)
	v_pk_add_f32 v[34:35], v[36:37], v[34:35]
	v_pk_add_f32 v[36:37], v[38:39], v[32:33]
	s_waitcnt lgkmcnt(1)
	v_pk_add_f32 v[38:39], v[40:41], v[26:27]
	v_pk_add_f32 v[40:41], v[42:43], v[24:25]
	ds_read_b128 v[24:27], v23 offset:17424
	s_waitcnt lgkmcnt(1)
	v_pk_add_f32 v[42:43], v[34:35], v[30:31]
	ds_read_b128 v[30:33], v23 offset:26112
	v_pk_add_f32 v[28:29], v[36:37], v[28:29]
	ds_read_b128 v[34:37], v23 offset:26128
	s_waitcnt lgkmcnt(2)
	v_pk_add_f32 v[40:41], v[40:41], v[24:25]
	v_pk_add_f32 v[38:39], v[38:39], v[26:27]
	s_waitcnt lgkmcnt(1)
	v_pk_add_f32 v[24:25], v[28:29], v[30:31]
	v_pk_add_f32 v[26:27], v[42:43], v[32:33]
	s_waitcnt lgkmcnt(0)
	v_pk_add_f32 v[28:29], v[40:41], v[34:35]
	v_pk_add_f32 v[30:31], v[38:39], v[36:37]
	s_waitcnt vmcnt(0)
	v_mul_f32_e32 v10, v28, v10
	v_fmac_f32_e32 v10, v24, v2
	v_mul_f32_e32 v14, v28, v14
	v_add_f32_e32 v2, 0, v10
	v_mul_f32_e32 v10, v29, v15
	v_fmac_f32_e32 v14, v24, v6
	v_fmac_f32_e32 v10, v25, v7
	v_mul_f32_e32 v7, v29, v11
	v_add_f32_e32 v6, 0, v14
	v_fmac_f32_e32 v7, v25, v3
	v_mul_f32_e32 v3, v30, v16
	v_add_f32_e32 v6, v6, v10
	v_fmac_f32_e32 v3, v26, v8
	v_add_f32_e32 v3, v6, v3
	v_mul_f32_e32 v6, v30, v12
	v_fmac_f32_e32 v6, v26, v4
	v_mul_f32_e32 v4, v31, v17
	v_fmac_f32_e32 v4, v27, v9
	v_add_f32_e32 v2, v2, v7
	v_add_f32_e32 v3, v3, v4
	v_mul_f32_e32 v4, v31, v13
	v_add_f32_e32 v2, v2, v6
	v_fmac_f32_e32 v4, v27, v5
	v_add_f32_e32 v2, v2, v4
	ds_write_b128 v23, v[24:27]
	ds_write_b128 v23, v[28:31] offset:16
	s_nop 1
	v_add_f32_dpp v3, v3, v3 quad_perm:[1,0,3,2] row_mask:0xf bank_mask:0xf
	v_add_f32_dpp v6, v2, v2 quad_perm:[1,0,3,2] row_mask:0xf bank_mask:0xf
	s_nop 1
	v_add_f32_dpp v3, v3, v3 quad_perm:[2,3,0,1] row_mask:0xf bank_mask:0xf
	v_add_f32_dpp v6, v6, v6 quad_perm:[2,3,0,1] row_mask:0xf bank_mask:0xf
	s_nop 1
	v_add_f32_dpp v2, v3, v3 row_half_mirror row_mask:0xf bank_mask:0xf
	v_add_f32_dpp v3, v6, v6 row_half_mirror row_mask:0xf bank_mask:0xf
	v_cmp_eq_u32_e32 vcc, 0, v1
	s_and_saveexec_b64 s[6:7], vcc
	s_cbranch_execz .LBB0_2
	v_mul_f32_e32 v4, 0x3f7d70a4, v3
	v_mul_f32_e32 v4, 0x3fb8aa3b, v4
	v_mul_f32_e32 v3, 0x3c23d70a, v3
	v_exp_f32_e32 v4, v4
	v_mul_f32_e32 v3, 0x3fb8aa3b, v3
	v_exp_f32_e32 v3, v3
	v_lshlrev_b32_e32 v5, 2, v22
	s_load_dwordx2 s[10:11], s[0:1], 0x38
	v_or_b32_e32 v6, 0x10a80, v5
	v_mul_f32_e32 v2, 0xbf7d70a4, v2
	ds_write_b32 v6, v4
	v_or_b32_e32 v4, 0x10a00, v5
	v_mul_f32_e32 v2, 0x3fb8aa3b, v2
	ds_write_b32 v4, v3
	v_exp_f32_e32 v4, v2
	v_add_u32_e32 v2, s3, v22
	v_ashrrev_i32_e32 v3, 31, v2
	s_waitcnt lgkmcnt(0)
	v_lshl_add_u64 v[2:3], v[2:3], 2, s[10:11]
	global_store_dword v[2:3], v4, off
